# baseline (speedup 1.0000x reference)
.Lmk_start:
	s_mov_b32 s28, s8
	s_mov_b64 s[30:31], s[4:5]
	s_mov_b64 s[32:33], s[6:7]
	s_mov_b64 s[6:7], s[2:3]
	s_mov_b64 s[34:35], s[2:3]
	s_mov_b32 s2, s28
	s_and_b32 s3, s2, 7
	s_lshr_b32 s4, s2, 3
	s_and_b32 s5, s4, 3
	s_lshl_b32 s3, s3, 2
	s_or_b32 s8, s3, s5
	s_lshr_b32 s9, s4, 2
	v_lshrrev_b32_e32 v127, 6, v0
	v_and_b32_e32 v124, 63, v0
	v_lshlrev_b32_e32 v124, 4, v124
	v_add_u32_e32 v125, 0xf000, v124
	v_readfirstlane_b32 s12, v127
	v_mov_b32_e32 v120, 0
	v_mov_b32_e32 v121, 0
	v_mov_b32_e32 v122, 0
	v_mov_b32_e32 v123, 0
	s_lshl_b32 s13, s12, 10
	s_lshl_b32 s14, s9, 3
	s_add_u32 s14, s14, s12
	s_mul_i32 s15, s14, 0x1800
	s_mul_i32 s16, s8, 0x12000
	s_add_u32 s16, s16, 0xc0000
	s_add_u32 s16, s16, s13
	s_add_u32 s20, s13, 0x2000
	s_add_u32 s10, s6, s16
	s_addc_u32 s11, s7, 0
	s_add_u32 s18, s6, s15
	s_addc_u32 s19, s7, 0
	s_add_u32 s22, s18, 0xc00
	s_addc_u32 s23, s19, 0
	s_cmp_lt_u32 s12, 4
	s_cbranch_scc0 .Lmk_vb
	s_mov_b32 m0, s13
	s_nop 0
	global_load_lds_dwordx4 v124, s[10:11]
	s_add_u32 s26, s10, 0x2000
	s_addc_u32 s27, s11, 0
	s_mov_b32 m0, s20
	s_nop 0
	global_load_lds_dwordx4 v124, s[26:27]
	global_load_dwordx4 v[96:99], v124, s[18:19]
	global_load_dwordx4 v[100:103], v124, s[18:19] offset:1024
	global_load_dwordx4 v[104:107], v124, s[18:19] offset:2048
	global_load_dwordx4 v[108:111], v124, s[22:23]
	global_load_dwordx4 v[112:115], v124, s[22:23] offset:1024
	global_load_dwordx4 v[116:119], v124, s[22:23] offset:2048
	s_add_u32 s24, s10, 0x3000
	s_addc_u32 s25, s11, 0
	s_add_u32 s26, s13, 0x3000
	s_mov_b32 m0, s26
	s_nop 0
	global_load_lds_dwordx4 v124, s[24:25]
	s_add_u32 s26, s24, 0x2000
	s_addc_u32 s27, s25, 0
	s_add_u32 s29, s20, 0x3000
	s_mov_b32 m0, s29
	s_nop 0
	global_load_lds_dwordx4 v124, s[26:27]
	s_add_u32 s24, s10, 0x6000
	s_addc_u32 s25, s11, 0
	s_add_u32 s26, s13, 0x6000
	s_mov_b32 m0, s26
	s_nop 0
	global_load_lds_dwordx4 v124, s[24:25]
	s_add_u32 s26, s24, 0x2000
	s_addc_u32 s27, s25, 0
	s_add_u32 s29, s20, 0x6000
	s_mov_b32 m0, s29
	s_nop 0
	global_load_lds_dwordx4 v124, s[26:27]
	s_add_u32 s24, s10, 0x9000
	s_addc_u32 s25, s11, 0
	s_add_u32 s26, s13, 0x9000
	s_mov_b32 m0, s26
	s_nop 0
	global_load_lds_dwordx4 v124, s[24:25]
	s_add_u32 s26, s24, 0x2000
	s_addc_u32 s27, s25, 0
	s_add_u32 s29, s20, 0x9000
	s_mov_b32 m0, s29
	s_nop 0
	global_load_lds_dwordx4 v124, s[26:27]
	s_add_u32 s24, s10, 0xc000
	s_addc_u32 s25, s11, 0
	s_add_u32 s26, s13, 0xc000
	s_mov_b32 m0, s26
	s_nop 0
	global_load_lds_dwordx4 v124, s[24:25]
	s_add_u32 s26, s24, 0x2000
	s_addc_u32 s27, s25, 0
	s_add_u32 s29, s20, 0xc000
	s_mov_b32 m0, s29
	s_nop 0
	global_load_lds_dwordx4 v124, s[26:27]
	s_waitcnt vmcnt(8)
	s_barrier
	ds_read_b128 v[0:3], v124
	ds_read_b128 v[4:7], v124 offset:1024
	ds_read_b128 v[8:11], v124 offset:2048
	ds_read_b128 v[12:15], v124 offset:3072
	ds_read_b128 v[16:19], v124 offset:4096
	ds_read_b128 v[20:23], v124 offset:5120
	s_waitcnt lgkmcnt(0)
	s_setprio 3
	v_mfma_f32_32x32x64_f8f6f4 v[48:63], v[0:5], v[96:101], 0 cbsz:2 blgp:2
	ds_read_b128 v[24:27], v124 offset:6144
	v_mfma_f32_32x32x64_f8f6f4 v[48:63], v[6:11], v[102:107], v[48:63] cbsz:2 blgp:2
	ds_read_b128 v[28:31], v124 offset:7168
	ds_read_b128 v[32:35], v124 offset:8192
	v_mfma_f32_32x32x64_f8f6f4 v[48:63], v[12:17], v[108:113], v[48:63] cbsz:2 blgp:2
	ds_read_b128 v[36:39], v124 offset:9216
	v_mfma_f32_32x32x64_f8f6f4 v[48:63], v[18:23], v[114:119], v[48:63] cbsz:2 blgp:2
	ds_read_b128 v[40:43], v124 offset:10240
	ds_read_b128 v[44:47], v124 offset:11264
	s_waitcnt vmcnt(0) lgkmcnt(0)
	s_barrier
	s_add_u32 s24, s10, 0xf000
	s_addc_u32 s25, s11, 0
	s_mov_b32 m0, s13
	s_nop 0
	global_load_lds_dwordx4 v124, s[24:25]
	s_add_u32 s26, s24, 0x2000
	s_addc_u32 s27, s25, 0
	s_mov_b32 m0, s20
	s_nop 0
	global_load_lds_dwordx4 v124, s[26:27]
	v_mfma_f32_32x32x64_f8f6f4 v[64:79], v[24:29], v[96:101], 0 cbsz:2 blgp:2
	ds_read_b128 v[0:3], v124 offset:12288
	ds_read_b128 v[4:7], v124 offset:13312
	ds_read_b128 v[8:11], v124 offset:14336
	ds_read_b128 v[24:27], v124 offset:18432
	v_mfma_f32_32x32x64_f8f6f4 v[64:79], v[30:35], v[102:107], v[64:79] cbsz:2 blgp:2
	ds_read_b128 v[12:15], v124 offset:15360
	ds_read_b128 v[16:19], v124 offset:16384
	ds_read_b128 v[20:23], v124 offset:17408
	ds_read_b128 v[28:31], v124 offset:19456
	ds_read_b128 v[32:35], v124 offset:20480
	v_exp_f32_e32 v48, v48
	v_exp_f32_e32 v49, v49
	v_exp_f32_e32 v50, v50
	v_exp_f32_e32 v51, v51
	v_mfma_f32_32x32x64_f8f6f4 v[64:79], v[36:41], v[108:113], v[64:79] cbsz:2 blgp:2
	ds_read_b128 v[36:39], v124 offset:21504
	v_exp_f32_e32 v52, v52
	v_exp_f32_e32 v53, v53
	v_exp_f32_e32 v54, v54
	v_exp_f32_e32 v55, v55
	v_pk_add_f32 v[120:121], v[120:121], v[48:49]
	v_pk_add_f32 v[122:123], v[122:123], v[50:51]
	v_mfma_f32_32x32x64_f8f6f4 v[64:79], v[42:47], v[114:119], v[64:79] cbsz:2 blgp:2
	ds_read_b128 v[40:43], v124 offset:22528
	ds_read_b128 v[44:47], v124 offset:23552
	v_exp_f32_e32 v56, v56
	v_exp_f32_e32 v57, v57
	v_exp_f32_e32 v58, v58
	v_exp_f32_e32 v59, v59
	v_pk_add_f32 v[120:121], v[120:121], v[52:53]
	v_pk_add_f32 v[122:123], v[122:123], v[54:55]
	s_waitcnt lgkmcnt(5)
	v_mfma_f32_32x32x64_f8f6f4 v[80:95], v[0:5], v[96:101], 0 cbsz:2 blgp:2
	ds_read_b128 v[0:3], v124 offset:24576
	v_exp_f32_e32 v60, v60
	v_exp_f32_e32 v61, v61
	v_exp_f32_e32 v62, v62
	v_exp_f32_e32 v63, v63
	v_pk_add_f32 v[120:121], v[120:121], v[56:57]
	v_pk_add_f32 v[122:123], v[122:123], v[58:59]
	v_mfma_f32_32x32x64_f8f6f4 v[80:95], v[6:11], v[102:107], v[80:95] cbsz:2 blgp:2
	ds_read_b128 v[4:7], v124 offset:25600
	ds_read_b128 v[8:11], v124 offset:26624
	v_exp_f32_e32 v64, v64
	v_exp_f32_e32 v65, v65
	v_exp_f32_e32 v66, v66
	v_exp_f32_e32 v67, v67
	v_pk_add_f32 v[120:121], v[120:121], v[60:61]
	v_pk_add_f32 v[122:123], v[122:123], v[62:63]
	v_mfma_f32_32x32x64_f8f6f4 v[80:95], v[12:17], v[108:113], v[80:95] cbsz:2 blgp:2
	ds_read_b128 v[12:15], v124 offset:27648
	v_exp_f32_e32 v68, v68
	v_exp_f32_e32 v69, v69
	v_exp_f32_e32 v70, v70
	v_exp_f32_e32 v71, v71
	v_pk_add_f32 v[120:121], v[120:121], v[64:65]
	v_pk_add_f32 v[122:123], v[122:123], v[66:67]
	v_mfma_f32_32x32x64_f8f6f4 v[80:95], v[18:23], v[114:119], v[80:95] cbsz:2 blgp:2
	ds_read_b128 v[16:19], v124 offset:28672
	ds_read_b128 v[20:23], v124 offset:29696
	v_exp_f32_e32 v72, v72
	v_exp_f32_e32 v73, v73
	v_exp_f32_e32 v74, v74
	v_exp_f32_e32 v75, v75
	v_pk_add_f32 v[120:121], v[120:121], v[68:69]
	v_pk_add_f32 v[122:123], v[122:123], v[70:71]
	s_waitcnt lgkmcnt(6)
	v_mfma_f32_32x32x64_f8f6f4 v[48:63], v[24:29], v[96:101], 0 cbsz:2 blgp:2
	ds_read_b128 v[24:27], v124 offset:30720
	v_exp_f32_e32 v76, v76
	v_exp_f32_e32 v77, v77
	v_exp_f32_e32 v78, v78
	v_exp_f32_e32 v79, v79
	v_pk_add_f32 v[120:121], v[120:121], v[72:73]
	v_pk_add_f32 v[122:123], v[122:123], v[74:75]
	v_mfma_f32_32x32x64_f8f6f4 v[48:63], v[30:35], v[102:107], v[48:63] cbsz:2 blgp:2
	ds_read_b128 v[28:31], v124 offset:31744
	ds_read_b128 v[32:35], v124 offset:32768
	v_exp_f32_e32 v80, v80
	v_exp_f32_e32 v81, v81
	v_exp_f32_e32 v82, v82
	v_exp_f32_e32 v83, v83
	v_pk_add_f32 v[120:121], v[120:121], v[76:77]
	v_pk_add_f32 v[122:123], v[122:123], v[78:79]
	v_mfma_f32_32x32x64_f8f6f4 v[48:63], v[36:41], v[108:113], v[48:63] cbsz:2 blgp:2
	ds_read_b128 v[36:39], v124 offset:33792
	v_exp_f32_e32 v84, v84
	v_exp_f32_e32 v85, v85
	v_exp_f32_e32 v86, v86
	v_exp_f32_e32 v87, v87
	v_pk_add_f32 v[120:121], v[120:121], v[80:81]
	v_pk_add_f32 v[122:123], v[122:123], v[82:83]
	v_mfma_f32_32x32x64_f8f6f4 v[48:63], v[42:47], v[114:119], v[48:63] cbsz:2 blgp:2
	ds_read_b128 v[40:43], v124 offset:34816
	ds_read_b128 v[44:47], v124 offset:35840
	v_exp_f32_e32 v88, v88
	v_exp_f32_e32 v89, v89
	v_exp_f32_e32 v90, v90
	v_exp_f32_e32 v91, v91
	v_pk_add_f32 v[120:121], v[120:121], v[84:85]
	v_pk_add_f32 v[122:123], v[122:123], v[86:87]
	s_setprio 2
	s_waitcnt lgkmcnt(6)
	v_mfma_f32_32x32x64_f8f6f4 v[64:79], v[0:5], v[96:101], 0 cbsz:2 blgp:2
	ds_read_b128 v[0:3], v124 offset:36864
	v_exp_f32_e32 v92, v92
	v_exp_f32_e32 v93, v93
	v_exp_f32_e32 v94, v94
	v_exp_f32_e32 v95, v95
	v_pk_add_f32 v[120:121], v[120:121], v[88:89]
	v_pk_add_f32 v[122:123], v[122:123], v[90:91]
	v_mfma_f32_32x32x64_f8f6f4 v[64:79], v[6:11], v[102:107], v[64:79] cbsz:2 blgp:2
	ds_read_b128 v[4:7], v124 offset:37888
	ds_read_b128 v[8:11], v124 offset:38912
	v_exp_f32_e32 v48, v48
	v_exp_f32_e32 v49, v49
	v_exp_f32_e32 v50, v50
	v_exp_f32_e32 v51, v51
	v_pk_add_f32 v[120:121], v[120:121], v[92:93]
	v_pk_add_f32 v[122:123], v[122:123], v[94:95]
	v_mfma_f32_32x32x64_f8f6f4 v[64:79], v[12:17], v[108:113], v[64:79] cbsz:2 blgp:2
	ds_read_b128 v[12:15], v124 offset:39936
	v_exp_f32_e32 v52, v52
	v_exp_f32_e32 v53, v53
	v_exp_f32_e32 v54, v54
	v_exp_f32_e32 v55, v55
	v_pk_add_f32 v[120:121], v[120:121], v[48:49]
	v_pk_add_f32 v[122:123], v[122:123], v[50:51]
	v_mfma_f32_32x32x64_f8f6f4 v[64:79], v[18:23], v[114:119], v[64:79] cbsz:2 blgp:2
	ds_read_b128 v[16:19], v124 offset:40960
	ds_read_b128 v[20:23], v124 offset:41984
	v_exp_f32_e32 v56, v56
	v_exp_f32_e32 v57, v57
	v_exp_f32_e32 v58, v58
	v_exp_f32_e32 v59, v59
	v_pk_add_f32 v[120:121], v[120:121], v[52:53]
	v_pk_add_f32 v[122:123], v[122:123], v[54:55]
	s_waitcnt lgkmcnt(6)
	v_mfma_f32_32x32x64_f8f6f4 v[80:95], v[24:29], v[96:101], 0 cbsz:2 blgp:2
	ds_read_b128 v[24:27], v124 offset:43008
	v_exp_f32_e32 v60, v60
	v_exp_f32_e32 v61, v61
	v_exp_f32_e32 v62, v62
	v_exp_f32_e32 v63, v63
	v_pk_add_f32 v[120:121], v[120:121], v[56:57]
	v_pk_add_f32 v[122:123], v[122:123], v[58:59]
	v_mfma_f32_32x32x64_f8f6f4 v[80:95], v[30:35], v[102:107], v[80:95] cbsz:2 blgp:2
	ds_read_b128 v[28:31], v124 offset:44032
	ds_read_b128 v[32:35], v124 offset:45056
	v_exp_f32_e32 v64, v64
	v_exp_f32_e32 v65, v65
	v_exp_f32_e32 v66, v66
	v_exp_f32_e32 v67, v67
	v_pk_add_f32 v[120:121], v[120:121], v[60:61]
	v_pk_add_f32 v[122:123], v[122:123], v[62:63]
	v_mfma_f32_32x32x64_f8f6f4 v[80:95], v[36:41], v[108:113], v[80:95] cbsz:2 blgp:2
	ds_read_b128 v[36:39], v124 offset:46080
	v_exp_f32_e32 v68, v68
	v_exp_f32_e32 v69, v69
	v_exp_f32_e32 v70, v70
	v_exp_f32_e32 v71, v71
	v_pk_add_f32 v[120:121], v[120:121], v[64:65]
	v_pk_add_f32 v[122:123], v[122:123], v[66:67]
	v_mfma_f32_32x32x64_f8f6f4 v[80:95], v[42:47], v[114:119], v[80:95] cbsz:2 blgp:2
	ds_read_b128 v[40:43], v124 offset:47104
	ds_read_b128 v[44:47], v124 offset:48128
	v_exp_f32_e32 v72, v72
	v_exp_f32_e32 v73, v73
	v_exp_f32_e32 v74, v74
	v_exp_f32_e32 v75, v75
	v_pk_add_f32 v[120:121], v[120:121], v[68:69]
	v_pk_add_f32 v[122:123], v[122:123], v[70:71]
	s_waitcnt lgkmcnt(6)
	v_mfma_f32_32x32x64_f8f6f4 v[48:63], v[0:5], v[96:101], 0 cbsz:2 blgp:2
	ds_read_b128 v[0:3], v124 offset:49152
	v_exp_f32_e32 v76, v76
	v_exp_f32_e32 v77, v77
	v_exp_f32_e32 v78, v78
	v_exp_f32_e32 v79, v79
	v_pk_add_f32 v[120:121], v[120:121], v[72:73]
	v_pk_add_f32 v[122:123], v[122:123], v[74:75]
	v_mfma_f32_32x32x64_f8f6f4 v[48:63], v[6:11], v[102:107], v[48:63] cbsz:2 blgp:2
	ds_read_b128 v[4:7], v124 offset:50176
	ds_read_b128 v[8:11], v124 offset:51200
	v_exp_f32_e32 v80, v80
	v_exp_f32_e32 v81, v81
	v_exp_f32_e32 v82, v82
	v_exp_f32_e32 v83, v83
	v_pk_add_f32 v[120:121], v[120:121], v[76:77]
	v_pk_add_f32 v[122:123], v[122:123], v[78:79]
	v_mfma_f32_32x32x64_f8f6f4 v[48:63], v[12:17], v[108:113], v[48:63] cbsz:2 blgp:2
	ds_read_b128 v[12:15], v124 offset:52224
	v_exp_f32_e32 v84, v84
	v_exp_f32_e32 v85, v85
	v_exp_f32_e32 v86, v86
	v_exp_f32_e32 v87, v87
	v_pk_add_f32 v[120:121], v[120:121], v[80:81]
	v_pk_add_f32 v[122:123], v[122:123], v[82:83]
	v_mfma_f32_32x32x64_f8f6f4 v[48:63], v[18:23], v[114:119], v[48:63] cbsz:2 blgp:2
	ds_read_b128 v[16:19], v124 offset:53248
	ds_read_b128 v[20:23], v124 offset:54272
	v_exp_f32_e32 v88, v88
	v_exp_f32_e32 v89, v89
	v_exp_f32_e32 v90, v90
	v_exp_f32_e32 v91, v91
	v_pk_add_f32 v[120:121], v[120:121], v[84:85]
	v_pk_add_f32 v[122:123], v[122:123], v[86:87]
	s_waitcnt lgkmcnt(6)
	v_mfma_f32_32x32x64_f8f6f4 v[64:79], v[24:29], v[96:101], 0 cbsz:2 blgp:2
	ds_read_b128 v[24:27], v124 offset:55296
	v_exp_f32_e32 v92, v92
	v_exp_f32_e32 v93, v93
	v_exp_f32_e32 v94, v94
	v_exp_f32_e32 v95, v95
	v_pk_add_f32 v[120:121], v[120:121], v[88:89]
	v_pk_add_f32 v[122:123], v[122:123], v[90:91]
	v_mfma_f32_32x32x64_f8f6f4 v[64:79], v[30:35], v[102:107], v[64:79] cbsz:2 blgp:2
	ds_read_b128 v[28:31], v124 offset:56320
	ds_read_b128 v[32:35], v124 offset:57344
	v_exp_f32_e32 v48, v48
	v_exp_f32_e32 v49, v49
	v_exp_f32_e32 v50, v50
	v_exp_f32_e32 v51, v51
	v_pk_add_f32 v[120:121], v[120:121], v[92:93]
	v_pk_add_f32 v[122:123], v[122:123], v[94:95]
	v_mfma_f32_32x32x64_f8f6f4 v[64:79], v[36:41], v[108:113], v[64:79] cbsz:2 blgp:2
	ds_read_b128 v[36:39], v124 offset:58368
	v_exp_f32_e32 v52, v52
	v_exp_f32_e32 v53, v53
	v_exp_f32_e32 v54, v54
	v_exp_f32_e32 v55, v55
	v_pk_add_f32 v[120:121], v[120:121], v[48:49]
	v_pk_add_f32 v[122:123], v[122:123], v[50:51]
	v_mfma_f32_32x32x64_f8f6f4 v[64:79], v[42:47], v[114:119], v[64:79] cbsz:2 blgp:2
	ds_read_b128 v[40:43], v124 offset:59392
	ds_read_b128 v[44:47], v124 offset:60416
	v_exp_f32_e32 v56, v56
	v_exp_f32_e32 v57, v57
	v_exp_f32_e32 v58, v58
	v_exp_f32_e32 v59, v59
	v_pk_add_f32 v[120:121], v[120:121], v[52:53]
	v_pk_add_f32 v[122:123], v[122:123], v[54:55]
	s_setprio 1
	s_waitcnt vmcnt(0) lgkmcnt(6)
	s_barrier
	v_mfma_f32_32x32x64_f8f6f4 v[80:95], v[0:5], v[96:101], 0 cbsz:2 blgp:2
	ds_read_b128 v[0:3], v124
	v_exp_f32_e32 v60, v60
	v_exp_f32_e32 v61, v61
	v_exp_f32_e32 v62, v62
	v_exp_f32_e32 v63, v63
	v_pk_add_f32 v[120:121], v[120:121], v[56:57]
	v_pk_add_f32 v[122:123], v[122:123], v[58:59]
	v_mfma_f32_32x32x64_f8f6f4 v[80:95], v[6:11], v[102:107], v[80:95] cbsz:2 blgp:2
	ds_read_b128 v[4:7], v124 offset:1024
	ds_read_b128 v[8:11], v124 offset:2048
	v_exp_f32_e32 v64, v64
	v_exp_f32_e32 v65, v65
	v_exp_f32_e32 v66, v66
	v_exp_f32_e32 v67, v67
	v_pk_add_f32 v[120:121], v[120:121], v[60:61]
	v_pk_add_f32 v[122:123], v[122:123], v[62:63]
	v_mfma_f32_32x32x64_f8f6f4 v[80:95], v[12:17], v[108:113], v[80:95] cbsz:2 blgp:2
	ds_read_b128 v[12:15], v124 offset:3072
	v_exp_f32_e32 v68, v68
	v_exp_f32_e32 v69, v69
	v_exp_f32_e32 v70, v70
	v_exp_f32_e32 v71, v71
	v_pk_add_f32 v[120:121], v[120:121], v[64:65]
	v_pk_add_f32 v[122:123], v[122:123], v[66:67]
	v_mfma_f32_32x32x64_f8f6f4 v[80:95], v[18:23], v[114:119], v[80:95] cbsz:2 blgp:2
	ds_read_b128 v[16:19], v124 offset:4096
	ds_read_b128 v[20:23], v124 offset:5120
	v_exp_f32_e32 v72, v72
	v_exp_f32_e32 v73, v73
	v_exp_f32_e32 v74, v74
	v_exp_f32_e32 v75, v75
	v_pk_add_f32 v[120:121], v[120:121], v[68:69]
	v_pk_add_f32 v[122:123], v[122:123], v[70:71]
	s_waitcnt lgkmcnt(6)
	v_mfma_f32_32x32x64_f8f6f4 v[48:63], v[24:29], v[96:101], 0 cbsz:2 blgp:2
	ds_read_b128 v[24:27], v124 offset:6144
	v_exp_f32_e32 v76, v76
	v_exp_f32_e32 v77, v77
	v_exp_f32_e32 v78, v78
	v_exp_f32_e32 v79, v79
	v_pk_add_f32 v[120:121], v[120:121], v[72:73]
	v_pk_add_f32 v[122:123], v[122:123], v[74:75]
	v_mfma_f32_32x32x64_f8f6f4 v[48:63], v[30:35], v[102:107], v[48:63] cbsz:2 blgp:2
	ds_read_b128 v[28:31], v124 offset:7168
	ds_read_b128 v[32:35], v124 offset:8192
	v_exp_f32_e32 v80, v80
	v_exp_f32_e32 v81, v81
	v_exp_f32_e32 v82, v82
	v_exp_f32_e32 v83, v83
	v_pk_add_f32 v[120:121], v[120:121], v[76:77]
	v_pk_add_f32 v[122:123], v[122:123], v[78:79]
	s_cmp_lg_u32 s8, 10
	s_cbranch_scc1 .Lmk_nosplit_a
	v_add_f32_e32 v127, v120, v121
	v_add_f32_e32 v126, v122, v123
	v_mov_b32_e32 v120, 0
	v_mov_b32_e32 v121, 0
	v_mov_b32_e32 v122, 0
	v_mov_b32_e32 v123, 0
	v_add_f32_e32 v127, v127, v126
